# v36: v34 + gate/up GEMM: 1/64 weight scale folded into the MFMA block scale (E8M0 0x79, exact), the 64 per-unit scale multiplies and their pairing copies removed from the silu*up epilogue
# speedup vs baseline: 1.0015x; 1.0015x over previous
.LBB0_1936:
	v_mbcnt_lo_u32_b32 v0, -1, 0
	v_mbcnt_hi_u32_b32 v0, -1, v0
	s_lshl_b32 s34, s59, 8
	v_ashrrev_i32_e32 v1, 1, v0
	v_bfi_b32 v2, -16, v1, v0
	v_and_b32_e32 v178, 16, v0
	v_mov_b32_e32 v5, v160
	v_mov_b32_e32 v160, v173
	v_mul_f32_e32 v0, 0xbfb8aa3b, v172
	v_exp_f32_e32 v0, v0
	s_add_i32 s34, s34, s50
	s_lshl_b32 s23, s30, 7
	v_add_f32_e32 v0, 1.0, v0
	v_rcp_f32_e32 v3, v0
	v_mul_f32_e32 v0, 0xbfb8aa3b, v173
	v_exp_f32_e32 v8, v0
	s_ashr_i32 s8, s23, 31
	v_mul_f32_e32 v3, v172, v3
	v_mul_f32_e32 v3, v3, v5
	v_add_f32_e32 v4, 1.0, v8
	v_rcp_f32_e32 v10, v4
	v_mov_b32_e32 v5, v162
	v_mov_b32_e32 v162, v175
	v_mul_f32_e32 v8, 0xbfb8aa3b, v174
	v_exp_f32_e32 v11, v8
	v_mul_f32_e32 v6, v173, v10
	s_mul_i32 s30, s34, 0x600
	v_add_f32_e32 v10, 1.0, v11
	v_rcp_f32_e32 v10, v10
	v_mul_f32_e32 v12, 0xbfb8aa3b, v175
	v_exp_f32_e32 v12, v12
	s_mul_hi_i32 s35, s34, 0x600
	v_mul_f32_e32 v4, v174, v10
	v_mul_f32_e32 v10, v4, v5
	v_add_f32_e32 v11, 1.0, v12
	v_mul_f32_e32 v12, v6, v161
	v_mov_b32_e32 v7, v152
	v_rcp_f32_e32 v11, v11
	v_mul_f32_e32 v4, 0xbfb8aa3b, v168
	v_exp_f32_e32 v5, v4
	s_nop 0
	v_cvt_pk_fp8_f32 v4, v3, v12
	v_mul_f32_e32 v8, v175, v11
	v_add_f32_e32 v3, 1.0, v5
	v_rcp_f32_e32 v3, v3
	v_mov_b32_e32 v152, v169
	v_mul_f32_e32 v11, v8, v163
	v_mul_f32_e32 v3, v168, v3
	v_mul_f32_e32 v5, 0xbfb8aa3b, v169
	v_exp_f32_e32 v5, v5
	v_mul_f32_e32 v3, v3, v7
	v_mov_b32_e32 v7, v154
	v_cvt_pk_fp8_f32 v4, v10, v11 op_sel:[0,0,1]
	v_mul_f32_e32 v10, 0xbfb8aa3b, v170
	v_mov_b32_e32 v154, v171
	v_add_f32_e32 v5, 1.0, v5
	v_exp_f32_e32 v12, v10
	v_rcp_f32_e32 v5, v5
	v_mul_f32_e32 v13, 0xbfb8aa3b, v171
	v_exp_f32_e32 v13, v13
	s_add_u32 s36, s48, s30
	v_mul_f32_e32 v5, v169, v5
	v_add_f32_e32 v8, 1.0, v12
	v_rcp_f32_e32 v8, v8
	v_add_f32_e32 v12, 1.0, v13
	v_rcp_f32_e32 v12, v12
	v_mul_f32_e32 v9, v5, v153
	v_mul_f32_e32 v5, v170, v8
	v_mul_f32_e32 v13, v5, v7
	v_mul_f32_e32 v5, v171, v12
	v_mul_f32_e32 v10, v5, v155
	s_nop 0
	v_mov_b32_e32 v7, v148
	v_mov_b32_e32 v148, v165
	v_cvt_pk_fp8_f32 v5, v3, v9
	v_mul_f32_e32 v11, 0xbfb8aa3b, v165
	v_exp_f32_e32 v11, v11
	v_mul_f32_e32 v3, 0xbfb8aa3b, v164
	v_exp_f32_e32 v3, v3
	v_cvt_pk_fp8_f32 v5, v13, v10 op_sel:[0,0,1]
	v_add_f32_e32 v10, 1.0, v11
	v_rcp_f32_e32 v12, v10
	v_mov_b32_e32 v11, v150
	v_add_f32_e32 v3, 1.0, v3
	v_rcp_f32_e32 v3, v3
	v_mul_f32_e32 v13, 0xbfb8aa3b, v166
	v_exp_f32_e32 v13, v13
	v_mov_b32_e32 v150, v167
	v_mul_f32_e32 v3, v164, v3
	v_mul_f32_e32 v3, v3, v7
	v_add_f32_e32 v7, 1.0, v13
	v_mul_f32_e32 v6, v165, v12
	v_rcp_f32_e32 v7, v7
	v_mul_f32_e32 v14, v6, v149
	v_mul_f32_e32 v8, 0xbfb8aa3b, v167
	v_exp_f32_e32 v8, v8
	v_mul_f32_e32 v6, v166, v7
	v_mul_f32_e32 v10, v6, v11
	v_add_f32_e32 v11, 1.0, v8
	v_mov_b32_e32 v9, v144
	v_rcp_f32_e32 v11, v11
	v_mul_f32_e32 v6, 0xbfb8aa3b, v156
	v_exp_f32_e32 v7, v6
	s_nop 0
	v_cvt_pk_fp8_f32 v6, v3, v14
	v_mov_b32_e32 v144, v157
	v_add_f32_e32 v3, 1.0, v7
	v_rcp_f32_e32 v3, v3
	v_mul_f32_e32 v7, v167, v11
	v_mul_f32_e32 v7, v7, v151
	v_mov_b32_e32 v13, v146
	v_cvt_pk_fp8_f32 v6, v10, v7 op_sel:[0,0,1]
	v_mul_f32_e32 v3, v156, v3
	v_mul_f32_e32 v8, 0xbfb8aa3b, v158
	v_mul_f32_e32 v7, 0xbfb8aa3b, v157
	v_exp_f32_e32 v8, v8
	v_exp_f32_e32 v7, v7
	v_mov_b32_e32 v146, v159
	v_mul_f32_e32 v3, v3, v9
	v_add_f32_e32 v8, 1.0, v8
	v_add_f32_e32 v7, 1.0, v7
	v_rcp_f32_e32 v14, v8
	v_rcp_f32_e32 v7, v7
	v_mul_f32_e32 v15, 0xbfb8aa3b, v159
	v_exp_f32_e32 v15, v15
	s_addc_u32 s35, s49, s35
	v_mul_f32_e32 v7, v157, v7
	v_mul_f32_e32 v10, v7, v145
	v_add_f32_e32 v7, 1.0, v15
	v_mul_f32_e32 v11, v158, v14
	v_rcp_f32_e32 v12, v7
	s_nop 0
	v_cvt_pk_fp8_f32 v7, v3, v10
	v_mul_f32_e32 v3, v11, v13
	v_mul_f32_e32 v8, v159, v12
	v_mul_f32_e32 v8, v8, v147
	v_cvt_pk_fp8_f32 v7, v3, v8 op_sel:[0,0,1]
	v_mov_b32_e32 v9, v136
	v_mov_b32_e32 v136, v141
	v_mul_f32_e32 v3, 0xbfb8aa3b, v140
	v_exp_f32_e32 v3, v3
	s_add_u32 s36, s36, s23
	s_addc_u32 s35, s35, s8
	v_mul_f32_e32 v14, 0xbfb8aa3b, v141
	s_add_u32 s36, s36, s51
	v_add_f32_e32 v3, 1.0, v3
	v_exp_f32_e32 v14, v14
	s_addc_u32 s37, s35, 0
	v_rcp_f32_e32 v3, v3
	v_lshl_add_u64 v[0:1], s[36:37], 0, v[178:179]
	v_permlane32_swap_b32_e32 v4, v6
	v_permlane32_swap_b32_e32 v5, v7
	s_nop 1
	v_permlane16_swap_b32_e32 v4, v5
	v_permlane16_swap_b32_e32 v6, v7
	v_mad_i64_i32 v[10:11], s[36:37], v2, s56, v[0:1]
	global_store_dwordx4 v[10:11], v[4:7], off
	v_mul_f32_e32 v3, v140, v3
	v_mul_f32_e32 v3, v3, v9
	v_add_f32_e32 v4, 1.0, v14
	v_rcp_f32_e32 v8, v4
	v_mov_b32_e32 v5, v138
	v_mov_b32_e32 v138, v143
	v_mul_f32_e32 v6, 0xbfb8aa3b, v142
	v_exp_f32_e32 v9, v6
	v_mul_f32_e32 v8, v141, v8
	v_mul_f32_e32 v10, 0xbfb8aa3b, v143
	v_add_f32_e32 v9, 1.0, v9
	v_rcp_f32_e32 v9, v9
	v_exp_f32_e32 v10, v10
	v_mul_f32_e32 v11, v8, v137
	s_addk_i32 s34, 0x80
	v_mul_f32_e32 v4, v142, v9
	v_mul_f32_e32 v12, v4, v5
	v_mov_b32_e32 v9, v128
	v_add_f32_e32 v10, 1.0, v10
	v_mul_f32_e32 v4, 0xbfb8aa3b, v132
	v_exp_f32_e32 v5, v4
	v_rcp_f32_e32 v10, v10
	s_nop 0
	v_cvt_pk_fp8_f32 v4, v3, v11
	v_add_f32_e32 v3, 1.0, v5
	v_rcp_f32_e32 v3, v3
	v_mul_f32_e32 v6, v143, v10
	v_mov_b32_e32 v128, v133
	v_mul_f32_e32 v10, v6, v139
	v_mul_f32_e32 v3, v132, v3
	v_mul_f32_e32 v5, 0xbfb8aa3b, v133
	v_exp_f32_e32 v5, v5
	v_mul_f32_e32 v3, v3, v9
	v_mov_b32_e32 v9, v130
	v_cvt_pk_fp8_f32 v4, v12, v10 op_sel:[0,0,1]
	v_mul_f32_e32 v10, 0xbfb8aa3b, v134
	v_mov_b32_e32 v130, v135
	v_add_f32_e32 v5, 1.0, v5
	v_exp_f32_e32 v12, v10
	v_rcp_f32_e32 v5, v5
	v_mul_f32_e32 v13, 0xbfb8aa3b, v135
	v_exp_f32_e32 v13, v13
	s_add_i32 s30, s30, 0x30000
	v_mul_f32_e32 v5, v133, v5
	v_add_f32_e32 v6, 1.0, v12
	v_rcp_f32_e32 v6, v6
	v_add_f32_e32 v12, 1.0, v13
	v_rcp_f32_e32 v12, v12
	v_mul_f32_e32 v7, v5, v129
	v_mul_f32_e32 v5, v134, v6
	v_mul_f32_e32 v13, v5, v9
	v_mul_f32_e32 v5, v135, v12
	v_mul_f32_e32 v10, v5, v131
	s_nop 0
	v_cvt_pk_fp8_f32 v5, v3, v7
	v_mov_b32_e32 v7, v124
	v_mov_b32_e32 v124, v121
	v_mul_f32_e32 v11, 0xbfb8aa3b, v121
	v_exp_f32_e32 v11, v11
	v_mul_f32_e32 v3, 0xbfb8aa3b, v120
	v_exp_f32_e32 v3, v3
	v_cvt_pk_fp8_f32 v5, v13, v10 op_sel:[0,0,1]
	v_add_f32_e32 v10, 1.0, v11
	v_rcp_f32_e32 v12, v10
	v_mov_b32_e32 v11, v126
	v_add_f32_e32 v3, 1.0, v3
	v_rcp_f32_e32 v3, v3
	v_mul_f32_e32 v13, 0xbfb8aa3b, v122
	v_exp_f32_e32 v13, v13
	v_mov_b32_e32 v126, v123
	v_mul_f32_e32 v3, v120, v3
	v_mul_f32_e32 v3, v3, v7
	v_add_f32_e32 v7, 1.0, v13
	v_mul_f32_e32 v6, v121, v12
	v_rcp_f32_e32 v7, v7
	v_mul_f32_e32 v14, v6, v125
	v_mul_f32_e32 v8, 0xbfb8aa3b, v123
	v_exp_f32_e32 v8, v8
	v_mul_f32_e32 v6, v122, v7
	v_mul_f32_e32 v10, v6, v11
	v_add_f32_e32 v11, 1.0, v8
	v_mov_b32_e32 v9, v116
	v_rcp_f32_e32 v11, v11
	v_mul_f32_e32 v6, 0xbfb8aa3b, v112
	v_exp_f32_e32 v7, v6
	s_nop 0
	v_cvt_pk_fp8_f32 v6, v3, v14
	v_mov_b32_e32 v116, v113
	v_add_f32_e32 v3, 1.0, v7
	v_rcp_f32_e32 v3, v3
	v_mul_f32_e32 v7, v123, v11
	v_mul_f32_e32 v7, v7, v127
	v_mov_b32_e32 v13, v118
	v_cvt_pk_fp8_f32 v6, v10, v7 op_sel:[0,0,1]
	v_mul_f32_e32 v3, v112, v3
	v_mul_f32_e32 v8, 0xbfb8aa3b, v114
	v_mul_f32_e32 v7, 0xbfb8aa3b, v113
	v_exp_f32_e32 v8, v8
	v_exp_f32_e32 v7, v7
	v_mov_b32_e32 v118, v115
	v_mul_f32_e32 v3, v3, v9
	v_add_f32_e32 v8, 1.0, v8
	v_add_f32_e32 v7, 1.0, v7
	v_rcp_f32_e32 v14, v8
	v_rcp_f32_e32 v7, v7
	v_mul_f32_e32 v15, 0xbfb8aa3b, v115
	v_exp_f32_e32 v15, v15
	v_permlane32_swap_b32_e32 v4, v6
	v_mul_f32_e32 v7, v113, v7
	v_mul_f32_e32 v10, v7, v117
	v_add_f32_e32 v7, 1.0, v15
	v_mul_f32_e32 v11, v114, v14
	v_rcp_f32_e32 v12, v7
	s_nop 0
	v_cvt_pk_fp8_f32 v7, v3, v10
	v_mul_f32_e32 v3, v11, v13
	v_mul_f32_e32 v8, v115, v12
	v_mul_f32_e32 v8, v8, v119
	v_cvt_pk_fp8_f32 v7, v3, v8 op_sel:[0,0,1]
	v_add_u32_e32 v14, 32, v2
	v_mad_i64_i32 v[0:1], s[36:37], v14, s56, v[0:1]
	v_permlane32_swap_b32_e32 v5, v7
	s_nop 1
	v_permlane16_swap_b32_e32 v4, v5
	v_permlane16_swap_b32_e32 v6, v7
	global_store_dwordx4 v[0:1], v[4:7], off
	s_nop 1
	v_mov_b32_e32 v5, v104
	v_mov_b32_e32 v104, v109
	v_mul_f32_e32 v0, 0xbfb8aa3b, v108
	v_exp_f32_e32 v0, v0
	s_mul_hi_i32 s34, s34, 0x600
	s_add_u32 s30, s48, s30
	v_add_f32_e32 v0, 1.0, v0
	v_rcp_f32_e32 v3, v0
	v_mul_f32_e32 v0, 0xbfb8aa3b, v109
	v_exp_f32_e32 v8, v0
	s_addc_u32 s34, s49, s34
	v_mul_f32_e32 v3, v108, v3
	v_mul_f32_e32 v3, v3, v5
	v_add_f32_e32 v4, 1.0, v8
	v_rcp_f32_e32 v10, v4
	v_mov_b32_e32 v5, v106
	v_mov_b32_e32 v106, v111
	v_mul_f32_e32 v8, 0xbfb8aa3b, v110
	v_exp_f32_e32 v11, v8
	v_mul_f32_e32 v6, v109, v10
	s_add_u32 s23, s30, s23
	v_add_f32_e32 v10, 1.0, v11
	v_rcp_f32_e32 v10, v10
	v_mul_f32_e32 v12, 0xbfb8aa3b, v111
	v_exp_f32_e32 v12, v12
	s_addc_u32 s8, s34, s8
	v_mul_f32_e32 v4, v110, v10
	v_mul_f32_e32 v10, v4, v5
	v_add_f32_e32 v11, 1.0, v12
	v_mul_f32_e32 v12, v6, v105
	v_mov_b32_e32 v7, v96
	v_rcp_f32_e32 v11, v11
	v_mul_f32_e32 v4, 0xbfb8aa3b, v100
	v_exp_f32_e32 v5, v4
	s_nop 0
	v_cvt_pk_fp8_f32 v4, v3, v12
	v_mul_f32_e32 v8, v111, v11
	v_add_f32_e32 v3, 1.0, v5
	v_rcp_f32_e32 v3, v3
	v_mov_b32_e32 v96, v101
	v_mul_f32_e32 v11, v8, v107
	v_mul_f32_e32 v3, v100, v3
	v_mul_f32_e32 v5, 0xbfb8aa3b, v101
	v_exp_f32_e32 v5, v5
	v_mul_f32_e32 v3, v3, v7
	v_mov_b32_e32 v7, v98
	v_cvt_pk_fp8_f32 v4, v10, v11 op_sel:[0,0,1]
	v_mul_f32_e32 v10, 0xbfb8aa3b, v102
	v_mov_b32_e32 v98, v103
	v_add_f32_e32 v5, 1.0, v5
	v_exp_f32_e32 v12, v10
	v_rcp_f32_e32 v5, v5
	v_mul_f32_e32 v13, 0xbfb8aa3b, v103
	v_exp_f32_e32 v13, v13
	s_add_u32 s34, s23, s51
	v_mul_f32_e32 v5, v101, v5
	v_add_f32_e32 v8, 1.0, v12
	v_rcp_f32_e32 v8, v8
	v_add_f32_e32 v12, 1.0, v13
	v_rcp_f32_e32 v12, v12
	v_mul_f32_e32 v9, v5, v97
	v_mul_f32_e32 v5, v102, v8
	v_mul_f32_e32 v13, v5, v7
	v_mul_f32_e32 v5, v103, v12
	v_mul_f32_e32 v10, v5, v99
	s_nop 0
	v_mov_b32_e32 v7, v88
	v_mov_b32_e32 v88, v93
	v_cvt_pk_fp8_f32 v5, v3, v9
	v_mul_f32_e32 v11, 0xbfb8aa3b, v93
	v_exp_f32_e32 v11, v11
	v_mul_f32_e32 v3, 0xbfb8aa3b, v92
	v_exp_f32_e32 v3, v3
	v_cvt_pk_fp8_f32 v5, v13, v10 op_sel:[0,0,1]
	v_add_f32_e32 v10, 1.0, v11
	v_rcp_f32_e32 v12, v10
	v_mov_b32_e32 v11, v90
	v_add_f32_e32 v3, 1.0, v3
	v_rcp_f32_e32 v3, v3
	v_mul_f32_e32 v13, 0xbfb8aa3b, v94
	v_exp_f32_e32 v13, v13
	v_mov_b32_e32 v90, v95
	v_mul_f32_e32 v3, v92, v3
	v_mul_f32_e32 v3, v3, v7
	v_add_f32_e32 v7, 1.0, v13
	v_mul_f32_e32 v6, v93, v12
	v_rcp_f32_e32 v7, v7
	v_mul_f32_e32 v15, v6, v89
	v_mul_f32_e32 v8, 0xbfb8aa3b, v95
	v_exp_f32_e32 v8, v8
	v_mul_f32_e32 v6, v94, v7
	v_mul_f32_e32 v10, v6, v11
	v_add_f32_e32 v11, 1.0, v8
	v_mov_b32_e32 v9, v80
	v_rcp_f32_e32 v11, v11
	v_mul_f32_e32 v6, 0xbfb8aa3b, v84
	v_exp_f32_e32 v7, v6
	s_nop 0
	v_cvt_pk_fp8_f32 v6, v3, v15
	v_mov_b32_e32 v80, v85
	v_add_f32_e32 v3, 1.0, v7
	v_rcp_f32_e32 v3, v3
	v_mul_f32_e32 v7, v95, v11
	v_mul_f32_e32 v7, v7, v91
	v_mov_b32_e32 v13, v82
	v_cvt_pk_fp8_f32 v6, v10, v7 op_sel:[0,0,1]
	v_mul_f32_e32 v3, v84, v3
	v_mul_f32_e32 v8, 0xbfb8aa3b, v86
	v_mul_f32_e32 v7, 0xbfb8aa3b, v85
	v_exp_f32_e32 v8, v8
	v_exp_f32_e32 v7, v7
	v_mov_b32_e32 v82, v87
	v_mul_f32_e32 v3, v3, v9
	v_add_f32_e32 v8, 1.0, v8
	v_add_f32_e32 v7, 1.0, v7
	v_rcp_f32_e32 v15, v8
	v_rcp_f32_e32 v7, v7
	v_mul_f32_e32 v16, 0xbfb8aa3b, v87
	v_exp_f32_e32 v16, v16
	s_addc_u32 s35, s8, 0
	v_mul_f32_e32 v7, v85, v7
	v_mul_f32_e32 v10, v7, v81
	v_add_f32_e32 v7, 1.0, v16
	v_mul_f32_e32 v11, v86, v15
	v_rcp_f32_e32 v12, v7
	s_nop 0
	v_cvt_pk_fp8_f32 v7, v3, v10
	v_mul_f32_e32 v3, v11, v13
	v_mul_f32_e32 v8, v87, v12
	v_mul_f32_e32 v8, v8, v83
	v_cvt_pk_fp8_f32 v7, v3, v8 op_sel:[0,0,1]
	v_mov_b32_e32 v9, v72
	v_mov_b32_e32 v72, v77
	v_mul_f32_e32 v3, 0xbfb8aa3b, v76
	v_exp_f32_e32 v10, v3
	v_lshl_add_u64 v[0:1], s[34:35], 0, v[178:179]
	v_permlane32_swap_b32_e32 v4, v6
	v_add_f32_e32 v10, 1.0, v10
	v_rcp_f32_e32 v12, v10
	v_permlane32_swap_b32_e32 v5, v7
	v_mul_f32_e32 v13, 0xbfb8aa3b, v77
	v_exp_f32_e32 v13, v13
	v_permlane16_swap_b32_e32 v4, v5
	v_permlane16_swap_b32_e32 v6, v7
	v_mad_i64_i32 v[2:3], s[34:35], v2, s56, v[0:1]
	global_store_dwordx4 v[2:3], v[4:7], off
	v_mul_f32_e32 v2, v76, v12
	v_mul_f32_e32 v8, v2, v9
	v_add_f32_e32 v2, 1.0, v13
	v_rcp_f32_e32 v6, v2
	v_mov_b32_e32 v3, v74
	v_mov_b32_e32 v74, v79
	v_mul_f32_e32 v4, 0xbfb8aa3b, v78
	v_exp_f32_e32 v7, v4
	v_mul_f32_e32 v6, v77, v6
	v_mul_f32_e32 v9, 0xbfb8aa3b, v79
	v_add_f32_e32 v7, 1.0, v7
	v_rcp_f32_e32 v7, v7
	v_exp_f32_e32 v9, v9
	v_mul_f32_e32 v10, v6, v73
	v_mad_i64_i32 v[0:1], s[34:35], v14, s56, v[0:1]
	v_mul_f32_e32 v2, v78, v7
	v_mul_f32_e32 v11, v2, v3
	v_mov_b32_e32 v7, v64
	v_add_f32_e32 v9, 1.0, v9
	v_mul_f32_e32 v2, 0xbfb8aa3b, v68
	v_exp_f32_e32 v3, v2
	v_rcp_f32_e32 v9, v9
	v_mov_b32_e32 v64, v69
	s_nop 0
	v_add_f32_e32 v3, 1.0, v3
	v_mul_f32_e32 v4, v79, v9
	v_rcp_f32_e32 v3, v3
	v_mul_f32_e32 v9, v4, v75
	v_cvt_pk_fp8_f32 v2, v8, v10
	v_mul_f32_e32 v8, 0xbfb8aa3b, v69
	v_exp_f32_e32 v8, v8
	v_mul_f32_e32 v3, v68, v3
	v_mul_f32_e32 v10, v3, v7
	v_mov_b32_e32 v7, v66
	v_add_f32_e32 v3, 1.0, v8
	v_mul_f32_e32 v8, 0xbfb8aa3b, v70
	v_mov_b32_e32 v66, v71
	v_cvt_pk_fp8_f32 v2, v11, v9 op_sel:[0,0,1]
	v_exp_f32_e32 v11, v8
	v_rcp_f32_e32 v3, v3
	v_mul_f32_e32 v12, 0xbfb8aa3b, v71
	v_exp_f32_e32 v12, v12
	s_and_b64 vcc, exec, s[24:25]
	v_mul_f32_e32 v3, v69, v3
	v_add_f32_e32 v4, 1.0, v11
	v_rcp_f32_e32 v4, v4
	v_add_f32_e32 v11, 1.0, v12
	v_rcp_f32_e32 v11, v11
	v_mul_f32_e32 v5, v3, v65
	v_mul_f32_e32 v3, v70, v4
	v_mul_f32_e32 v12, v3, v7
	v_mul_f32_e32 v3, v71, v11
	v_mul_f32_e32 v8, v3, v67
	s_nop 0
	v_cvt_pk_fp8_f32 v3, v10, v5
	v_mov_b32_e32 v5, v56
	v_mov_b32_e32 v56, v61
	v_mul_f32_e32 v6, 0xbfb8aa3b, v60
	v_exp_f32_e32 v9, v6
	v_cvt_pk_fp8_f32 v3, v12, v8 op_sel:[0,0,1]
	v_mul_f32_e32 v10, 0xbfb8aa3b, v61
	v_exp_f32_e32 v10, v10
	v_add_f32_e32 v8, 1.0, v9
	v_rcp_f32_e32 v11, v8
	v_mov_b32_e32 v9, v58
	v_add_f32_e32 v8, 1.0, v10
	v_rcp_f32_e32 v10, v8
	v_mul_f32_e32 v4, v60, v11
	v_mul_f32_e32 v12, 0xbfb8aa3b, v62
	v_exp_f32_e32 v12, v12
	v_mul_f32_e32 v13, v4, v5
	v_mov_b32_e32 v58, v63
	v_mul_f32_e32 v4, v61, v10
	v_add_f32_e32 v5, 1.0, v12
	v_rcp_f32_e32 v5, v5
	v_mul_f32_e32 v12, v4, v57
	v_mul_f32_e32 v6, 0xbfb8aa3b, v63
	v_exp_f32_e32 v6, v6
	v_mul_f32_e32 v4, v62, v5
	v_mul_f32_e32 v8, v4, v9
	v_add_f32_e32 v9, 1.0, v6
	v_mov_b32_e32 v7, v48
	v_rcp_f32_e32 v9, v9
	v_mul_f32_e32 v4, 0xbfb8aa3b, v52
	v_exp_f32_e32 v5, v4
	s_nop 0
	v_cvt_pk_fp8_f32 v4, v13, v12
	v_mul_f32_e32 v9, v63, v9
	v_add_f32_e32 v5, 1.0, v5
	v_rcp_f32_e32 v5, v5
	v_mul_f32_e32 v9, v9, v59
	v_mov_b32_e32 v48, v53
	v_mov_b32_e32 v11, v50
	v_cvt_pk_fp8_f32 v4, v8, v9 op_sel:[0,0,1]
	v_mul_f32_e32 v5, v52, v5
	v_mul_f32_e32 v6, 0xbfb8aa3b, v53
	v_mul_f32_e32 v12, 0xbfb8aa3b, v54
	v_exp_f32_e32 v6, v6
	v_exp_f32_e32 v12, v12
	v_mul_f32_e32 v13, v5, v7
	v_mov_b32_e32 v50, v55
	v_add_f32_e32 v5, 1.0, v6
	v_add_f32_e32 v6, 1.0, v12
	v_rcp_f32_e32 v12, v6
	v_mov_b32_e32 v7, v51
	v_rcp_f32_e32 v5, v5
	v_mul_f32_e32 v15, 0xbfb8aa3b, v55
	v_exp_f32_e32 v15, v15
	v_permlane32_swap_b32_e32 v2, v4
	v_mul_f32_e32 v5, v53, v5
	v_mul_f32_e32 v8, v5, v49
	v_add_f32_e32 v5, 1.0, v15
	v_mul_f32_e32 v9, v54, v12
	v_rcp_f32_e32 v10, v5
	s_nop 0
	v_cvt_pk_fp8_f32 v5, v13, v8
	v_mul_f32_e32 v8, v9, v11
	v_mul_f32_e32 v6, v55, v10
	v_mul_f32_e32 v6, v6, v51
	v_cvt_pk_fp8_f32 v5, v8, v6 op_sel:[0,0,1]
	s_mov_b32 s59, s58
	s_mov_b32 s30, s22
	s_mov_b64 s[36:37], s[26:27]
	v_permlane32_swap_b32_e32 v3, v5
	s_nop 1
	v_permlane16_swap_b32_e32 v2, v3
	v_permlane16_swap_b32_e32 v4, v5
	global_store_dwordx4 v[0:1], v[2:5], off
	s_cbranch_vccnz .LBB0_1947
